# expert-counter loads issued together (moe tables, combine); router and combine loops software-pipelined (next token's row/index loads in flight during current token)
# speedup vs baseline: 1.0147x; 1.0001x over previous
.LBB0_1619:
	s_or_b64 exec, exec, s[0:1]
	s_mov_b64 exec, 0xffff
	v_mbcnt_lo_u32_b32 v80, -1, 0
	v_mbcnt_hi_u32_b32 v80, -1, v80
	s_lshl_b32 s98, s91, 9
	s_add_i32 s98, s98, 0x10000
	v_lshl_add_u32 v80, v80, 5, s98
	v_mov_b32_e32 v81, 0xff
	ds_write_b32 v80, v81
	s_mov_b64 exec, -1
	s_lshl_b32 s0, s13, 3
	s_add_i32 s56, s0, s91
	s_cmpk_gt_i32 s56, 0x3fff
	s_waitcnt vmcnt(16) lgkmcnt(0)
	s_barrier
	s_cbranch_scc1 .LBB0_1624
	s_lshl_b32 s58, s12, 3
	s_add_u32 s68, s52, 0x300000
	s_addc_u32 s69, s53, 0
	s_add_u32 s70, s52, 0x380000
	s_addc_u32 s71, s53, 0
	s_add_u32 s2, s52, 0x420000
	s_addc_u32 s3, s53, 0
	s_add_u32 s4, s52, 0x440000
	s_addc_u32 s5, s53, 0
	s_ashr_i32 s57, s56, 31
	s_lshl_b64 s[0:1], s[56:57], 2
	s_add_u32 s8, s0, 0x400000
	v_and_b32_e32 v0, 63, v0
	s_addc_u32 s9, s1, 0
	s_lshl_b64 s[0:1], s[56:57], 12
	s_ashr_i32 s59, s58, 31
	v_lshl_or_b32 v18, v0, 3, s0
	v_mov_b32_e32 v19, s1
	s_lshl_b32 s0, s13, 4
	v_readlane_b32 s1, v254, 53
	v_cmp_eq_u32_e64 s[36:37], 0, v0
	v_lshl_add_u32 v25, v0, 4, 0
	s_lshl_b64 s[72:73], s[58:59], 2
	s_lshl_b64 s[76:77], s[58:59], 12
	s_add_i32 s66, s1, s0
	s_lshl_b32 s12, s12, 4
	s_lshl_b32 s99, s91, 9
	s_add_i32 s99, s99, 0x10000
	s_mov_b64 s[18:19], 0x2d000000
	v_lshl_add_u64 v[78:79], s[52:53], 0, v[18:19]
	v_lshl_add_u64 v[78:79], v[78:79], 0, s[18:19]
	global_load_dwordx2 v[60:61], v[78:79], off
	global_load_dwordx2 v[62:63], v[78:79], off offset:512
	global_load_dwordx2 v[64:65], v[78:79], off offset:1024
	global_load_dwordx2 v[66:67], v[78:79], off offset:1536
	global_load_dwordx2 v[68:69], v[78:79], off offset:2048
	global_load_dwordx2 v[70:71], v[78:79], off offset:2560
	global_load_dwordx2 v[72:73], v[78:79], off offset:3072
	global_load_dwordx2 v[74:75], v[78:79], off offset:3584
	v_lshl_add_u64 v[78:79], v[78:79], 0, s[76:77]
	s_branch .LBB0_1622

.LBB0_1622:
	s_waitcnt lgkmcnt(0)
	s_waitcnt vmcnt(7)
	v_mov_b32_e32 v0, v60
	v_mov_b32_e32 v1, v61
	v_lshlrev_b32_e32 v26, 16, v0
	v_and_b32_e32 v28, 0xffff0000, v0
	v_lshlrev_b32_e32 v30, 16, v1
	v_and_b32_e32 v32, 0xffff0000, v1
	ds_read_b128 v[0:3], v25
	ds_read_b128 v[4:7], v25 offset:32768
	v_mul_f32_e32 v40, v28, v28
	v_fmac_f32_e32 v40, v26, v26
	v_fmac_f32_e32 v40, v30, v30
	s_waitcnt lgkmcnt(1)
	v_fma_f32 v39, v2, v26, 0
	v_fma_f32 v37, v3, v26, 0
	s_waitcnt lgkmcnt(0)
	v_fma_f32 v35, v4, v26, 0
	v_fma_f32 v33, v5, v26, 0
	v_fma_f32 v31, v6, v26, 0
	v_fma_f32 v29, v7, v26, 0
	ds_read_b128 v[2:5], v25 offset:8192
	ds_read_b128 v[6:9], v25 offset:40960
	v_pk_fma_f32 v[0:1], v[0:1], v[26:27], 0 op_sel_hi:[1,0,0]
	v_fmac_f32_e32 v40, v32, v32
	s_waitcnt lgkmcnt(1)
	v_fmac_f32_e32 v39, v4, v28
	v_fmac_f32_e32 v37, v5, v28
	s_waitcnt lgkmcnt(0)
	v_fmac_f32_e32 v35, v6, v28
	v_fmac_f32_e32 v33, v7, v28
	v_fmac_f32_e32 v31, v8, v28
	v_fmac_f32_e32 v29, v9, v28
	ds_read_b128 v[4:7], v25 offset:16384
	ds_read_b128 v[8:11], v25 offset:49152
	s_waitcnt lgkmcnt(1)
	v_fmac_f32_e32 v39, v6, v30
	v_fmac_f32_e32 v37, v7, v30
	s_waitcnt lgkmcnt(0)
	v_fmac_f32_e32 v35, v8, v30
	v_fmac_f32_e32 v33, v9, v30
	v_fmac_f32_e32 v31, v10, v30
	v_fmac_f32_e32 v29, v11, v30
	ds_read_b128 v[6:9], v25 offset:24576
	ds_read_b128 v[10:13], v25 offset:57344
	s_waitcnt lgkmcnt(1)
	v_fmac_f32_e32 v39, v8, v32
	v_fmac_f32_e32 v37, v9, v32
	s_waitcnt lgkmcnt(0)
	v_fmac_f32_e32 v35, v10, v32
	v_fmac_f32_e32 v33, v11, v32
	v_fmac_f32_e32 v31, v12, v32
	v_fmac_f32_e32 v29, v13, v32
	v_pk_fma_f32 v[0:1], v[2:3], v[28:29], v[0:1] op_sel_hi:[1,0,1]
	s_waitcnt vmcnt(6)
	v_mov_b32_e32 v8, v62
	v_mov_b32_e32 v9, v63
	v_lshlrev_b32_e32 v34, 16, v8
	v_and_b32_e32 v16, 0xffff0000, v8
	v_lshlrev_b32_e32 v22, 16, v9
	v_and_b32_e32 v24, 0xffff0000, v9
	ds_read_b128 v[8:11], v25 offset:1024
	ds_read_b128 v[12:15], v25 offset:33792
	v_pk_fma_f32 v[0:1], v[4:5], v[30:31], v[0:1] op_sel_hi:[1,0,1]
	v_fmac_f32_e32 v40, v34, v34
	v_pk_fma_f32 v[0:1], v[6:7], v[32:33], v[0:1] op_sel_hi:[1,0,1]
	s_waitcnt lgkmcnt(1)
	v_fmac_f32_e32 v39, v10, v34
	v_pk_fma_f32 v[26:27], v[8:9], v[34:35], v[0:1] op_sel_hi:[1,0,1]
	ds_read_b128 v[0:3], v25 offset:9216
	ds_read_b128 v[4:7], v25 offset:41984
	v_fmac_f32_e32 v37, v11, v34
	s_waitcnt lgkmcnt(2)
	v_fmac_f32_e32 v35, v12, v34
	v_fmac_f32_e32 v33, v13, v34
	v_fmac_f32_e32 v31, v14, v34
	v_fmac_f32_e32 v29, v15, v34
	s_waitcnt lgkmcnt(1)
	v_fmac_f32_e32 v39, v2, v16
	v_fmac_f32_e32 v37, v3, v16
	s_waitcnt lgkmcnt(0)
	v_fmac_f32_e32 v35, v4, v16
	v_fmac_f32_e32 v33, v5, v16
	v_fmac_f32_e32 v31, v6, v16
	v_fmac_f32_e32 v29, v7, v16
	ds_read_b128 v[2:5], v25 offset:17408
	ds_read_b128 v[6:9], v25 offset:50176
	v_pk_fma_f32 v[0:1], v[0:1], v[16:17], v[26:27] op_sel_hi:[1,0,1]
	v_fmac_f32_e32 v40, v16, v16
	v_fmac_f32_e32 v40, v22, v22
	s_waitcnt lgkmcnt(1)
	v_fmac_f32_e32 v39, v4, v22
	v_fmac_f32_e32 v37, v5, v22
	s_waitcnt lgkmcnt(0)
	v_fmac_f32_e32 v35, v6, v22
	v_fmac_f32_e32 v33, v7, v22
	v_fmac_f32_e32 v31, v8, v22
	v_fmac_f32_e32 v29, v9, v22
	ds_read_b128 v[4:7], v25 offset:25600
	ds_read_b128 v[8:11], v25 offset:58368
	v_pk_fma_f32 v[0:1], v[2:3], v[22:23], v[0:1] op_sel_hi:[1,0,1]
	v_fmac_f32_e32 v40, v24, v24
	s_waitcnt lgkmcnt(1)
	v_fmac_f32_e32 v39, v6, v24
	v_fmac_f32_e32 v37, v7, v24
	s_waitcnt lgkmcnt(0)
	v_fmac_f32_e32 v35, v8, v24
	v_fmac_f32_e32 v33, v9, v24
	v_fmac_f32_e32 v31, v10, v24
	v_fmac_f32_e32 v29, v11, v24
	v_pk_fma_f32 v[0:1], v[4:5], v[24:25], v[0:1] op_sel_hi:[1,0,1]
	s_waitcnt vmcnt(5)
	v_mov_b32_e32 v6, v64
	v_mov_b32_e32 v7, v65
	v_lshlrev_b32_e32 v28, 16, v6
	v_and_b32_e32 v30, 0xffff0000, v6
	v_lshlrev_b32_e32 v32, 16, v7
	v_and_b32_e32 v34, 0xffff0000, v7
	ds_read_b128 v[6:9], v25 offset:2048
	ds_read_b128 v[10:13], v25 offset:34816
	v_fmac_f32_e32 v40, v28, v28
	v_fmac_f32_e32 v40, v30, v30
	v_fmac_f32_e32 v40, v32, v32
	s_waitcnt lgkmcnt(1)
	v_fmac_f32_e32 v39, v8, v28
	v_fmac_f32_e32 v37, v9, v28
	s_waitcnt lgkmcnt(0)
	v_fmac_f32_e32 v35, v10, v28
	v_fmac_f32_e32 v33, v11, v28
	v_fmac_f32_e32 v31, v12, v28
	v_fmac_f32_e32 v29, v13, v28
	ds_read_b128 v[8:11], v25 offset:10240
	ds_read_b128 v[12:15], v25 offset:43008
	v_fmac_f32_e32 v40, v34, v34
	s_waitcnt lgkmcnt(1)
	v_fmac_f32_e32 v39, v10, v30
	v_fmac_f32_e32 v37, v11, v30
	s_waitcnt lgkmcnt(0)
	v_fmac_f32_e32 v35, v12, v30
	v_fmac_f32_e32 v33, v13, v30
	ds_read_b128 v[10:13], v25 offset:18432
	ds_read_b128 v[42:45], v25 offset:51200
	v_fmac_f32_e32 v31, v14, v30
	v_fmac_f32_e32 v29, v15, v30
	s_waitcnt lgkmcnt(1)
	v_fmac_f32_e32 v39, v12, v32
	v_fmac_f32_e32 v37, v13, v32
	s_waitcnt lgkmcnt(0)
	v_fmac_f32_e32 v35, v42, v32
	v_fmac_f32_e32 v33, v43, v32
	v_fmac_f32_e32 v31, v44, v32
	v_fmac_f32_e32 v29, v45, v32
	ds_read_b128 v[12:15], v25 offset:26624
	ds_read_b128 v[42:45], v25 offset:59392
	s_waitcnt lgkmcnt(1)
	v_fmac_f32_e32 v39, v14, v34
	v_fmac_f32_e32 v37, v15, v34
	s_waitcnt lgkmcnt(0)
	v_fmac_f32_e32 v35, v42, v34
	v_fmac_f32_e32 v33, v43, v34
	v_fmac_f32_e32 v31, v44, v34
	v_fmac_f32_e32 v29, v45, v34
	ds_read_b128 v[42:45], v25 offset:3072
	ds_read_b128 v[46:49], v25 offset:35840
	s_waitcnt vmcnt(4)
	v_mov_b32_e32 v14, v66
	v_mov_b32_e32 v15, v67
	v_lshlrev_b32_e32 v36, 16, v14
	s_waitcnt lgkmcnt(1)
	v_fmac_f32_e32 v39, v44, v36
	v_fmac_f32_e32 v37, v45, v36
	s_waitcnt lgkmcnt(0)
	v_fmac_f32_e32 v35, v46, v36
	v_fmac_f32_e32 v33, v47, v36
	v_fmac_f32_e32 v31, v48, v36
	v_fmac_f32_e32 v29, v49, v36
	ds_read_b128 v[44:47], v25 offset:11264
	ds_read_b128 v[48:51], v25 offset:44032
	v_and_b32_e32 v14, 0xffff0000, v14
	v_lshlrev_b32_e32 v38, 16, v15
	v_and_b32_e32 v56, 0xffff0000, v15
	s_waitcnt lgkmcnt(1)
	v_fmac_f32_e32 v39, v46, v14
	v_fmac_f32_e32 v37, v47, v14
	s_waitcnt lgkmcnt(0)
	v_fmac_f32_e32 v35, v48, v14
	v_fmac_f32_e32 v33, v49, v14
	v_fmac_f32_e32 v31, v50, v14
	v_fmac_f32_e32 v29, v51, v14
	ds_read_b128 v[46:49], v25 offset:19456
	ds_read_b128 v[50:53], v25 offset:52224
	v_fmac_f32_e32 v40, v36, v36
	v_fmac_f32_e32 v40, v14, v14
	v_fmac_f32_e32 v40, v38, v38
	s_waitcnt lgkmcnt(1)
	v_fmac_f32_e32 v39, v48, v38
	s_waitcnt lgkmcnt(0)
	v_fmac_f32_e32 v29, v53, v38
	v_fmac_f32_e32 v31, v52, v38
	v_pk_fma_f32 v[0:1], v[6:7], v[28:29], v[0:1] op_sel_hi:[1,0,1]
	v_fmac_f32_e32 v33, v51, v38
	v_pk_fma_f32 v[0:1], v[8:9], v[30:31], v[0:1] op_sel_hi:[1,0,1]
	v_fmac_f32_e32 v35, v50, v38
	v_pk_fma_f32 v[0:1], v[10:11], v[32:33], v[0:1] op_sel_hi:[1,0,1]
	v_fmac_f32_e32 v37, v49, v38
	ds_read_b128 v[48:51], v25 offset:27648
	ds_read_b128 v[52:55], v25 offset:60416
	v_pk_fma_f32 v[0:1], v[12:13], v[34:35], v[0:1] op_sel_hi:[1,0,1]
	v_fmac_f32_e32 v40, v56, v56
	v_pk_fma_f32 v[0:1], v[42:43], v[36:37], v[0:1] op_sel_hi:[1,0,1]
	s_waitcnt lgkmcnt(1)
	v_fmac_f32_e32 v37, v51, v56
	v_pk_fma_f32 v[0:1], v[44:45], v[14:15], v[0:1] op_sel_hi:[1,0,1]
	s_waitcnt lgkmcnt(0)
	v_fmac_f32_e32 v35, v52, v56
	v_pk_fma_f32 v[0:1], v[46:47], v[38:39], v[0:1] op_sel_hi:[1,0,1]
	v_fmac_f32_e32 v39, v50, v56
	v_pk_fma_f32 v[22:23], v[48:49], v[56:57], v[0:1] op_sel_hi:[1,0,1]
	v_fmac_f32_e32 v33, v53, v56
	v_fmac_f32_e32 v31, v54, v56
	v_fmac_f32_e32 v29, v55, v56
	s_waitcnt vmcnt(3)
	v_mov_b32_e32 v0, v68
	v_mov_b32_e32 v1, v69
	v_lshlrev_b32_e32 v24, 16, v0
	v_and_b32_e32 v26, 0xffff0000, v0
	v_lshlrev_b32_e32 v28, 16, v1
	v_and_b32_e32 v30, 0xffff0000, v1
	ds_read_b128 v[0:3], v25 offset:4096
	ds_read_b128 v[4:7], v25 offset:36864
	v_fmac_f32_e32 v40, v24, v24
	v_fmac_f32_e32 v40, v26, v26
	v_fmac_f32_e32 v40, v28, v28
	s_waitcnt lgkmcnt(1)
	v_fmac_f32_e32 v39, v2, v24
	v_fmac_f32_e32 v37, v3, v24
	s_waitcnt lgkmcnt(0)
	v_fmac_f32_e32 v35, v4, v24
	v_fmac_f32_e32 v33, v5, v24
	v_fmac_f32_e32 v31, v6, v24
	v_fmac_f32_e32 v29, v7, v24
	ds_read_b128 v[2:5], v25 offset:12288
	ds_read_b128 v[6:9], v25 offset:45056
	v_pk_fma_f32 v[0:1], v[0:1], v[24:25], v[22:23] op_sel_hi:[1,0,1]
	v_fmac_f32_e32 v40, v30, v30
	s_waitcnt lgkmcnt(1)
	v_fmac_f32_e32 v39, v4, v26
	v_fmac_f32_e32 v37, v5, v26
	s_waitcnt lgkmcnt(0)
	v_fmac_f32_e32 v35, v6, v26
	v_fmac_f32_e32 v33, v7, v26
	v_fmac_f32_e32 v31, v8, v26
	v_fmac_f32_e32 v29, v9, v26
	ds_read_b128 v[4:7], v25 offset:20480
	ds_read_b128 v[8:11], v25 offset:53248
	v_pk_fma_f32 v[0:1], v[2:3], v[26:27], v[0:1] op_sel_hi:[1,0,1]
	s_waitcnt lgkmcnt(1)
	v_fmac_f32_e32 v39, v6, v28
	v_fmac_f32_e32 v37, v7, v28
	s_waitcnt lgkmcnt(0)
	v_fmac_f32_e32 v35, v8, v28
	v_fmac_f32_e32 v33, v9, v28
	v_fmac_f32_e32 v31, v10, v28
	v_fmac_f32_e32 v29, v11, v28
	ds_read_b128 v[6:9], v25 offset:28672
	ds_read_b128 v[10:13], v25 offset:61440
	s_waitcnt lgkmcnt(1)
	v_fmac_f32_e32 v39, v8, v30
	v_fmac_f32_e32 v37, v9, v30
	s_waitcnt lgkmcnt(0)
	v_fmac_f32_e32 v35, v10, v30
	v_fmac_f32_e32 v33, v11, v30
	v_fmac_f32_e32 v31, v12, v30
	v_fmac_f32_e32 v29, v13, v30
	s_waitcnt vmcnt(2)
	v_mov_b32_e32 v8, v70
	v_mov_b32_e32 v9, v71
	v_lshlrev_b32_e32 v32, 16, v8
	v_and_b32_e32 v34, 0xffff0000, v8
	v_lshlrev_b32_e32 v36, 16, v9
	v_and_b32_e32 v38, 0xffff0000, v9
	ds_read_b128 v[8:11], v25 offset:5120
	ds_read_b128 v[12:15], v25 offset:37888
	v_fmac_f32_e32 v40, v32, v32
	v_fmac_f32_e32 v40, v34, v34
	v_fmac_f32_e32 v40, v36, v36
	s_waitcnt lgkmcnt(1)
	v_fmac_f32_e32 v39, v10, v32
	v_fmac_f32_e32 v37, v11, v32
	s_waitcnt lgkmcnt(0)
	v_fmac_f32_e32 v35, v12, v32
	v_fmac_f32_e32 v33, v13, v32
	v_fmac_f32_e32 v31, v14, v32
	v_fmac_f32_e32 v29, v15, v32
	ds_read_b128 v[10:13], v25 offset:13312
	ds_read_b128 v[14:17], v25 offset:46080
	v_fmac_f32_e32 v40, v38, v38
	s_waitcnt lgkmcnt(1)
	v_fmac_f32_e32 v39, v12, v34
	v_fmac_f32_e32 v37, v13, v34
	s_waitcnt lgkmcnt(0)
	v_fmac_f32_e32 v35, v14, v34
	v_fmac_f32_e32 v33, v15, v34
	ds_read_b128 v[12:15], v25 offset:21504
	ds_read_b128 v[42:45], v25 offset:54272
	v_fmac_f32_e32 v31, v16, v34
	v_fmac_f32_e32 v29, v17, v34
	s_waitcnt lgkmcnt(1)
	v_fmac_f32_e32 v39, v14, v36
	v_fmac_f32_e32 v37, v15, v36
	s_waitcnt lgkmcnt(0)
	v_fmac_f32_e32 v35, v42, v36
	v_fmac_f32_e32 v33, v43, v36
	v_fmac_f32_e32 v31, v44, v36
	v_fmac_f32_e32 v29, v45, v36
	ds_read_b128 v[14:17], v25 offset:29696
	ds_read_b128 v[42:45], v25 offset:62464
	s_waitcnt lgkmcnt(1)
	v_fmac_f32_e32 v39, v16, v38
	v_fmac_f32_e32 v37, v17, v38
	s_waitcnt lgkmcnt(0)
	v_fmac_f32_e32 v35, v42, v38
	v_fmac_f32_e32 v33, v43, v38
	v_fmac_f32_e32 v31, v44, v38
	v_fmac_f32_e32 v29, v45, v38
	ds_read_b128 v[42:45], v25 offset:6144
	ds_read_b128 v[46:49], v25 offset:38912
	s_waitcnt vmcnt(1)
	v_mov_b32_e32 v16, v72
	v_mov_b32_e32 v17, v73
	v_lshlrev_b32_e32 v54, 16, v16
	s_waitcnt lgkmcnt(1)
	v_fmac_f32_e32 v39, v44, v54
	v_fmac_f32_e32 v37, v45, v54
	s_waitcnt lgkmcnt(0)
	v_fmac_f32_e32 v35, v46, v54
	v_fmac_f32_e32 v33, v47, v54
	v_fmac_f32_e32 v31, v48, v54
	v_fmac_f32_e32 v29, v49, v54
	ds_read_b128 v[44:47], v25 offset:14336
	ds_read_b128 v[48:51], v25 offset:47104
	v_and_b32_e32 v56, 0xffff0000, v16
	v_lshlrev_b32_e32 v58, 16, v17
	v_and_b32_e32 v16, 0xffff0000, v17
	s_waitcnt lgkmcnt(1)
	v_fmac_f32_e32 v37, v47, v56
	s_waitcnt lgkmcnt(0)
	v_fmac_f32_e32 v29, v51, v56
	v_fmac_f32_e32 v31, v50, v56
	v_pk_fma_f32 v[0:1], v[4:5], v[28:29], v[0:1] op_sel_hi:[1,0,1]
	v_fmac_f32_e32 v33, v49, v56
	v_pk_fma_f32 v[0:1], v[6:7], v[30:31], v[0:1] op_sel_hi:[1,0,1]
	v_fmac_f32_e32 v35, v48, v56
	v_pk_fma_f32 v[0:1], v[8:9], v[32:33], v[0:1] op_sel_hi:[1,0,1]
	v_fmac_f32_e32 v39, v46, v56
	v_pk_fma_f32 v[0:1], v[10:11], v[34:35], v[0:1] op_sel_hi:[1,0,1]
	ds_read_b128 v[46:49], v25 offset:22528
	ds_read_b128 v[50:53], v25 offset:55296
	v_pk_fma_f32 v[0:1], v[12:13], v[36:37], v[0:1] op_sel_hi:[1,0,1]
	v_fmac_f32_e32 v40, v54, v54
	v_pk_fma_f32 v[0:1], v[14:15], v[38:39], v[0:1] op_sel_hi:[1,0,1]
	s_waitcnt lgkmcnt(1)
	v_fmac_f32_e32 v39, v48, v58
	v_pk_fma_f32 v[0:1], v[42:43], v[54:55], v[0:1] op_sel_hi:[1,0,1]
	v_fmac_f32_e32 v37, v49, v58
	v_pk_fma_f32 v[0:1], v[44:45], v[56:57], v[0:1] op_sel_hi:[1,0,1]
	s_waitcnt lgkmcnt(0)
	v_fmac_f32_e32 v35, v50, v58
	v_pk_fma_f32 v[12:13], v[46:47], v[58:59], v[0:1] op_sel_hi:[1,0,1]
	ds_read_b128 v[0:3], v25 offset:30720
	ds_read_b128 v[4:7], v25 offset:63488
	v_fmac_f32_e32 v33, v51, v58
	v_fmac_f32_e32 v31, v52, v58
	v_fmac_f32_e32 v29, v53, v58
	s_waitcnt lgkmcnt(1)
	v_fmac_f32_e32 v39, v2, v16
	v_fmac_f32_e32 v37, v3, v16
	s_waitcnt lgkmcnt(0)
	v_fmac_f32_e32 v35, v4, v16
	v_fmac_f32_e32 v33, v5, v16
	v_fmac_f32_e32 v31, v6, v16
	v_fmac_f32_e32 v29, v7, v16
	v_fmac_f32_e32 v40, v56, v56
	v_fmac_f32_e32 v40, v58, v58
	v_fmac_f32_e32 v40, v16, v16
	s_waitcnt vmcnt(0)
	v_mov_b32_e32 v2, v74
	v_mov_b32_e32 v3, v75
	global_load_dwordx2 v[60:61], v[78:79], off
	global_load_dwordx2 v[62:63], v[78:79], off offset:512
	global_load_dwordx2 v[64:65], v[78:79], off offset:1024
	global_load_dwordx2 v[66:67], v[78:79], off offset:1536
	global_load_dwordx2 v[68:69], v[78:79], off offset:2048
	global_load_dwordx2 v[70:71], v[78:79], off offset:2560
	global_load_dwordx2 v[72:73], v[78:79], off offset:3072
	global_load_dwordx2 v[74:75], v[78:79], off offset:3584
	v_lshl_add_u64 v[78:79], v[78:79], 0, s[76:77]
	v_lshlrev_b32_e32 v24, 16, v2
	v_and_b32_e32 v22, 0xffff0000, v2
	v_lshlrev_b32_e32 v20, 16, v3
	v_and_b32_e32 v14, 0xffff0000, v3
	ds_read_b128 v[2:5], v25 offset:7168
	ds_read_b128 v[6:9], v25 offset:39936
	v_fmac_f32_e32 v40, v24, v24
	v_fmac_f32_e32 v40, v22, v22
	v_fmac_f32_e32 v40, v20, v20
	s_waitcnt lgkmcnt(1)
	v_fmac_f32_e32 v39, v4, v24
	v_fmac_f32_e32 v37, v5, v24
	s_waitcnt lgkmcnt(0)
	v_fmac_f32_e32 v35, v6, v24
	v_fmac_f32_e32 v33, v7, v24
	v_fmac_f32_e32 v31, v8, v24
	v_fmac_f32_e32 v29, v9, v24
	ds_read_b128 v[4:7], v25 offset:15360
	ds_read_b128 v[8:11], v25 offset:48128
	v_fmac_f32_e32 v40, v14, v14
	s_waitcnt lgkmcnt(1)
	v_fmac_f32_e32 v39, v6, v22
	v_fmac_f32_e32 v37, v7, v22
	s_waitcnt lgkmcnt(0)
	v_fmac_f32_e32 v35, v8, v22
	v_fmac_f32_e32 v33, v9, v22
	ds_read_b128 v[6:9], v25 offset:23552
	ds_read_b128 v[42:45], v25 offset:56320
	v_fmac_f32_e32 v31, v10, v22
	v_fmac_f32_e32 v29, v11, v22
	s_waitcnt lgkmcnt(1)
	v_fmac_f32_e32 v39, v8, v20
	v_fmac_f32_e32 v37, v9, v20
	s_waitcnt lgkmcnt(0)
	v_fmac_f32_e32 v35, v42, v20
	v_fmac_f32_e32 v33, v43, v20
	v_fmac_f32_e32 v31, v44, v20
	v_fmac_f32_e32 v29, v45, v20
	ds_read_b128 v[8:11], v25 offset:31744
	ds_read_b128 v[42:45], v25 offset:64512
	s_waitcnt lgkmcnt(1)
	v_fmac_f32_e32 v39, v10, v14
	v_mbcnt_lo_u32_b32 v10, -1, 0
	v_mbcnt_hi_u32_b32 v10, -1, v10
	v_fmac_f32_e32 v37, v11, v14
	v_lshlrev_b32_e32 v10, 2, v10
	v_xor_b32_e32 v10, 4, v10
	ds_bpermute_b32 v10, v10, v40
	v_mbcnt_lo_u32_b32 v11, -1, 0
	v_mbcnt_hi_u32_b32 v11, -1, v11
	s_waitcnt lgkmcnt(1)
	v_fmac_f32_e32 v35, v42, v14
	v_lshlrev_b32_e32 v11, 2, v11
	v_xor_b32_e32 v11, 8, v11
	s_waitcnt lgkmcnt(0)
	v_add_f32_e32 v10, v40, v10
	ds_bpermute_b32 v11, v11, v10
	v_fmac_f32_e32 v33, v43, v14
	v_fmac_f32_e32 v31, v44, v14
	v_fmac_f32_e32 v29, v45, v14
	s_waitcnt lgkmcnt(0)
	v_add_f32_e32 v10, v10, v11
	v_mbcnt_lo_u32_b32 v11, -1, 0
	v_mbcnt_hi_u32_b32 v11, -1, v11
	s_nop 0
	v_lshlrev_b32_e32 v11, 2, v11
	v_xor_b32_e32 v11, 16, v11
	ds_bpermute_b32 v11, v11, v10
	s_waitcnt lgkmcnt(0)
	v_add_f32_e32 v10, v10, v11
	v_mbcnt_lo_u32_b32 v11, -1, 0
	v_mbcnt_hi_u32_b32 v11, -1, v11
	s_nop 0
	v_lshlrev_b32_e32 v11, 2, v11
	v_xor_b32_e32 v11, 32, v11
	ds_bpermute_b32 v11, v11, v10
	s_waitcnt lgkmcnt(0)
	v_add_f32_e32 v10, v10, v11
	v_mbcnt_lo_u32_b32 v11, -1, 0
	v_mbcnt_hi_u32_b32 v11, -1, v11
	s_nop 0
	v_lshlrev_b32_e32 v11, 2, v11
	v_xor_b32_e32 v11, 64, v11
	ds_bpermute_b32 v11, v11, v10
	s_waitcnt lgkmcnt(0)
	v_add_f32_e32 v10, v10, v11
	v_mbcnt_lo_u32_b32 v11, -1, 0
	v_mbcnt_hi_u32_b32 v11, -1, v11
	v_mbcnt_lo_u32_b32 v15, -1, 0
	v_mbcnt_hi_u32_b32 v15, -1, v15
	v_mbcnt_lo_u32_b32 v17, -1, 0
	v_mbcnt_hi_u32_b32 v17, -1, v17
	v_mbcnt_lo_u32_b32 v21, -1, 0
	v_mbcnt_hi_u32_b32 v21, -1, v21
	v_mbcnt_lo_u32_b32 v23, -1, 0
	v_mbcnt_hi_u32_b32 v23, -1, v23
	v_mbcnt_lo_u32_b32 v26, -1, 0
	v_mbcnt_hi_u32_b32 v26, -1, v26
	v_mbcnt_lo_u32_b32 v27, -1, 0
	v_mbcnt_hi_u32_b32 v27, -1, v27
	s_nop 0
	v_lshlrev_b32_e32 v15, 2, v15
	v_lshlrev_b32_e32 v17, 2, v17
	v_xor_b32_e32 v17, 8, v17
	v_lshlrev_b32_e32 v23, 2, v23
	v_pk_fma_f32 v[0:1], v[0:1], v[16:17], v[12:13] op_sel_hi:[1,0,1]
	v_lshlrev_b32_e32 v21, 2, v21
	v_xor_b32_e32 v23, 32, v23
	v_pk_fma_f32 v[0:1], v[2:3], v[24:25], v[0:1] op_sel_hi:[1,0,1]
	v_xor_b32_e32 v21, 16, v21
	v_mbcnt_lo_u32_b32 v28, -1, 0
	v_mbcnt_hi_u32_b32 v28, -1, v28
	v_pk_fma_f32 v[0:1], v[4:5], v[22:23], v[0:1] op_sel_hi:[1,0,1]
	v_xor_b32_e32 v15, 4, v15
	v_lshlrev_b32_e32 v28, 2, v28
	v_pk_fma_f32 v[0:1], v[6:7], v[20:21], v[0:1] op_sel_hi:[1,0,1]
	v_xor_b32_e32 v28, 4, v28
	v_pk_fma_f32 v[0:1], v[8:9], v[14:15], v[0:1] op_sel_hi:[1,0,1]
	v_mbcnt_lo_u32_b32 v41, -1, 0
	v_mbcnt_hi_u32_b32 v41, -1, v41
	v_lshlrev_b32_e32 v41, 2, v41
	v_xor_b32_e32 v42, 4, v41
	ds_bpermute_b32 v2, v42, v0
	ds_bpermute_b32 v3, v42, v1
	ds_bpermute_b32 v43, v42, v39
	ds_bpermute_b32 v44, v42, v37
	ds_bpermute_b32 v45, v42, v35
	ds_bpermute_b32 v46, v42, v33
	ds_bpermute_b32 v47, v42, v31
	ds_bpermute_b32 v48, v42, v29
	s_waitcnt lgkmcnt(0)
	v_pk_add_f32 v[0:1], v[0:1], v[2:3]
	v_add_f32_e32 v39, v39, v43
	v_add_f32_e32 v37, v37, v44
	v_add_f32_e32 v35, v35, v45
	v_add_f32_e32 v33, v33, v46
	v_add_f32_e32 v31, v31, v47
	v_add_f32_e32 v29, v29, v48
	v_xor_b32_e32 v42, 8, v41
	ds_bpermute_b32 v2, v42, v0
	ds_bpermute_b32 v3, v42, v1
	ds_bpermute_b32 v43, v42, v39
	ds_bpermute_b32 v44, v42, v37
	ds_bpermute_b32 v45, v42, v35
	ds_bpermute_b32 v46, v42, v33
	ds_bpermute_b32 v47, v42, v31
	ds_bpermute_b32 v48, v42, v29
	s_waitcnt lgkmcnt(0)
	v_pk_add_f32 v[0:1], v[0:1], v[2:3]
	v_add_f32_e32 v39, v39, v43
	v_add_f32_e32 v37, v37, v44
	v_add_f32_e32 v35, v35, v45
	v_add_f32_e32 v33, v33, v46
	v_add_f32_e32 v31, v31, v47
	v_add_f32_e32 v29, v29, v48
	v_xor_b32_e32 v42, 16, v41
	ds_bpermute_b32 v2, v42, v0
	ds_bpermute_b32 v3, v42, v1
	ds_bpermute_b32 v43, v42, v39
	ds_bpermute_b32 v44, v42, v37
	ds_bpermute_b32 v45, v42, v35
	ds_bpermute_b32 v46, v42, v33
	ds_bpermute_b32 v47, v42, v31
	ds_bpermute_b32 v48, v42, v29
	s_waitcnt lgkmcnt(0)
	v_pk_add_f32 v[0:1], v[0:1], v[2:3]
	v_add_f32_e32 v39, v39, v43
	v_add_f32_e32 v37, v37, v44
	v_add_f32_e32 v35, v35, v45
	v_add_f32_e32 v33, v33, v46
	v_add_f32_e32 v31, v31, v47
	v_add_f32_e32 v29, v29, v48
	v_xor_b32_e32 v42, 32, v41
	ds_bpermute_b32 v2, v42, v0
	ds_bpermute_b32 v3, v42, v1
	ds_bpermute_b32 v43, v42, v39
	ds_bpermute_b32 v44, v42, v37
	ds_bpermute_b32 v45, v42, v35
	ds_bpermute_b32 v46, v42, v33
	ds_bpermute_b32 v47, v42, v31
	ds_bpermute_b32 v48, v42, v29
	s_waitcnt lgkmcnt(0)
	v_pk_add_f32 v[0:1], v[0:1], v[2:3]
	v_add_f32_e32 v39, v39, v43
	v_add_f32_e32 v37, v37, v44
	v_add_f32_e32 v35, v35, v45
	v_add_f32_e32 v33, v33, v46
	v_add_f32_e32 v31, v31, v47
	v_add_f32_e32 v29, v29, v48
	v_xor_b32_e32 v42, 64, v41
	ds_bpermute_b32 v2, v42, v0
	ds_bpermute_b32 v3, v42, v1
	ds_bpermute_b32 v43, v42, v39
	ds_bpermute_b32 v44, v42, v37
	ds_bpermute_b32 v45, v42, v35
	ds_bpermute_b32 v46, v42, v33
	ds_bpermute_b32 v47, v42, v31
	ds_bpermute_b32 v48, v42, v29
	s_waitcnt lgkmcnt(0)
	v_pk_add_f32 v[0:1], v[0:1], v[2:3]
	v_add_f32_e32 v39, v39, v43
	v_add_f32_e32 v37, v37, v44
	v_add_f32_e32 v35, v35, v45
	v_add_f32_e32 v33, v33, v46
	v_add_f32_e32 v31, v31, v47
	v_add_f32_e32 v29, v29, v48
	v_xor_b32_e32 v42, 0x80, v41
	ds_bpermute_b32 v2, v42, v0
	ds_bpermute_b32 v3, v42, v1
	ds_bpermute_b32 v11, v42, v10
	ds_bpermute_b32 v6, v42, v39
	ds_bpermute_b32 v8, v42, v37
	ds_bpermute_b32 v12, v42, v35
	ds_bpermute_b32 v14, v42, v33
	ds_bpermute_b32 v16, v42, v31
	ds_bpermute_b32 v20, v42, v29
	v_mov_b32_e32 v5, v39
	v_mov_b32_e32 v7, v37
	v_mov_b32_e32 v9, v35
	v_mov_b32_e32 v13, v33
	v_mov_b32_e32 v15, v31
	v_mov_b32_e32 v17, v29
	s_waitcnt lgkmcnt(0)
	s_and_saveexec_b64 s[0:1], s[36:37]
	s_cbranch_execz .LBB0_1621
	v_add_f32_e32 v4, v10, v11
	v_fmamk_f32 v4, v4, 0x3a000000, v253
	s_mov_b32 s13, 0xf800000
	v_cmp_gt_f32_e32 vcc, s13, v4
	v_mul_f32_e32 v10, 0x4f800000, v4
	v_add_f32_e32 v5, v5, v6
	v_cndmask_b32_e32 v4, v4, v10, vcc
	v_sqrt_f32_e32 v10, v4
	v_pk_add_f32 v[0:1], v[0:1], v[2:3]
	v_add_f32_e32 v7, v7, v8
	v_add_f32_e32 v9, v9, v12
	v_add_u32_e32 v11, -1, v10
	v_fma_f32 v21, -v11, v10, v4
	v_cmp_ge_f32_e64 s[38:39], 0, v21
	v_add_u32_e32 v21, 1, v10
	v_add_f32_e32 v13, v13, v14
	v_cndmask_b32_e64 v11, v10, v11, s[38:39]
	v_fma_f32 v10, -v21, v10, v4
	v_cmp_lt_f32_e64 s[38:39], 0, v10
	s_nop 1
	v_cndmask_b32_e64 v10, v11, v21, s[38:39]
	v_mul_f32_e32 v11, 0x37800000, v10
	v_cndmask_b32_e32 v10, v10, v11, vcc
	v_mov_b32_e32 v11, 0x260
	v_cmp_class_f32_e32 vcc, v4, v11
	s_nop 1
	v_cndmask_b32_e32 v4, v10, v4, vcc
	v_div_scale_f32 v10, s[18:19], v4, v4, 1.0
	v_rcp_f32_e32 v11, v10
	s_nop 0
	v_fma_f32 v21, -v10, v11, 1.0
	v_fmac_f32_e32 v11, v21, v11
	v_div_scale_f32 v21, vcc, 1.0, v4, 1.0
	v_mul_f32_e32 v22, v21, v11
	v_fma_f32 v23, -v10, v22, v21
	v_fmac_f32_e32 v22, v23, v11
	v_fma_f32 v10, -v10, v22, v21
	v_div_fmas_f32 v10, v10, v11, v22
	v_div_fixup_f32 v4, v10, v4, 1.0
	v_mul_f32_e32 v5, v4, v5
	v_pk_mul_f32 v[0:1], v[4:5], v[0:1] op_sel_hi:[0,1]
	v_cmp_gt_f32_e32 vcc, v1, v0
	v_mul_f32_e32 v7, v4, v7
	v_mul_f32_e32 v9, v4, v9
	v_cndmask_b32_e32 v2, v0, v1, vcc
	v_cmp_gt_f32_e64 s[38:39], v5, v2
	v_mul_f32_e32 v13, v4, v13
	v_cndmask_b32_e64 v3, 0, 1, vcc
	v_cndmask_b32_e64 v2, v2, v5, s[38:39]
	v_cmp_gt_f32_e64 s[40:41], v7, v2
	v_add_f32_e32 v11, v15, v16
	v_cndmask_b32_e64 v3, v3, 2, s[38:39]
	v_cndmask_b32_e64 v2, v2, v7, s[40:41]
	v_cmp_gt_f32_e64 s[42:43], v9, v2
	v_mul_f32_e32 v11, v4, v11
	v_cndmask_b32_e64 v3, v3, 3, s[40:41]
	v_cndmask_b32_e64 v2, v2, v9, s[42:43]
	v_cmp_gt_f32_e64 s[44:45], v13, v2
	s_waitcnt lgkmcnt(0)
	v_add_f32_e32 v10, v17, v20
	v_cndmask_b32_e64 v3, v3, 4, s[42:43]
	v_cndmask_b32_e64 v2, v2, v13, s[44:45]
	v_cmp_gt_f32_e64 s[46:47], v11, v2
	v_mul_f32_e32 v10, v4, v10
	v_cndmask_b32_e64 v3, v3, 5, s[44:45]
	v_cndmask_b32_e64 v2, v2, v11, s[46:47]
	v_cmp_ngt_f32_e64 s[48:49], v10, v2
	v_cndmask_b32_e64 v3, v3, 6, s[46:47]
	s_and_b64 s[18:19], s[48:49], s[46:47]
	v_cndmask_b32_e64 v176, 7, v3, s[48:49]
	v_cmp_ne_u32_e64 s[46:47], 0, v176
	v_cmp_lt_f32_e64 s[50:51], s11, v0
	s_and_b64 s[46:47], s[46:47], s[50:51]
	v_mov_b32_e32 v3, 0xff61b1e6
	v_cndmask_b32_e64 v0, v3, v0, s[46:47]
	v_cmp_ne_u32_e64 s[44:45], 1, v176
	v_cmp_gt_f32_e64 s[46:47], v1, v0
	s_and_b64 s[44:45], s[44:45], s[46:47]
	v_cndmask_b32_e64 v0, v0, v1, s[44:45]
	v_cmp_ne_u32_e64 s[42:43], 2, v176
	v_cmp_gt_f32_e64 s[46:47], v5, v0
	s_and_b64 s[42:43], s[42:43], s[46:47]
	v_cndmask_b32_e64 v0, v0, v5, s[42:43]
	v_cmp_ne_u32_e64 s[40:41], 3, v176
	v_cmp_gt_f32_e64 s[46:47], v7, v0
	s_and_b64 s[40:41], s[40:41], s[46:47]
	v_cndmask_b32_e64 v0, v0, v7, s[40:41]
	v_cmp_ne_u32_e64 s[38:39], 4, v176
	v_cmp_gt_f32_e64 s[46:47], v9, v0
	s_and_b64 s[38:39], s[38:39], s[46:47]
	v_cndmask_b32_e64 v0, v0, v9, s[38:39]
	v_cmp_ne_u32_e32 vcc, 5, v176
	v_cmp_gt_f32_e64 s[46:47], v13, v0
	s_and_b64 vcc, vcc, s[46:47]
	v_cndmask_b32_e32 v0, v0, v13, vcc
	v_cmp_ngt_f32_e64 s[46:47], v11, v0
	s_or_b64 s[46:47], s[18:19], s[46:47]
	v_cndmask_b32_e64 v2, v10, v2, s[48:49]
	v_cndmask_b32_e64 v1, v11, v0, s[46:47]
	v_cmp_gt_f32_e64 s[50:51], v10, v1
	s_and_b64 s[50:51], s[48:49], s[50:51]
	v_cndmask_b32_e64 v0, 0, 1, s[44:45]
	v_cndmask_b32_e64 v1, v1, v10, s[50:51]
	v_sub_f32_e32 v1, v2, v1
	v_mul_f32_e32 v1, 0x3fb8aa3b, v1
	v_exp_f32_e32 v1, v1
	v_cndmask_b32_e64 v0, v0, 2, s[42:43]
	v_cndmask_b32_e64 v0, v0, 3, s[40:41]
	v_cndmask_b32_e64 v0, v0, 4, s[38:39]
	v_add_f32_e32 v1, 1.0, v1
	v_div_scale_f32 v2, s[18:19], v1, v1, 1.0
	v_rcp_f32_e32 v3, v2
	v_cndmask_b32_e64 v0, v0, 5, vcc
	s_add_u32 s18, s52, s8
	s_addc_u32 s19, s53, s9
	v_fma_f32 v5, -v2, v3, 1.0
	v_fmac_f32_e32 v3, v5, v3
	v_div_scale_f32 v5, vcc, 1.0, v1, 1.0
	v_mul_f32_e32 v6, v5, v3
	v_fma_f32 v7, -v2, v6, v5
	v_fmac_f32_e32 v6, v7, v3
	v_fma_f32 v2, -v2, v6, v5
	v_div_fmas_f32 v2, v2, v3, v6
	v_div_fixup_f32 v5, v2, v1, 1.0
	v_cndmask_b32_e64 v0, 6, v0, s[46:47]
	v_cndmask_b32_e64 v0, v0, 7, s[50:51]
	v_sub_f32_e32 v10, 1.0, v5
	v_mov_b32_e32 v80, v176
	v_mov_b32_e32 v81, v0
	v_mov_b32_e32 v82, v4
	v_mov_b32_e32 v83, v10
	v_mov_b32_e32 v84, v5
	v_mov_b32_e32 v85, s56
	v_mov_b32_e32 v6, s99
	ds_write_b128 v6, v[80:83]
	ds_write_b64 v6, v[84:85] offset:16
	s_add_i32 s99, s99, 32
	s_branch .LBB0_1621

.LBB0_1674:
	s_andn2_b64 vcc, exec, s[0:1]
	s_cbranch_vccnz .LBB0_1790
	v_mbcnt_lo_u32_b32 v0, -1, 0
	v_mbcnt_hi_u32_b32 v0, -1, v0
	v_readlane_b32 s0, v254, 2
	v_add_u32_e32 v0, s79, v0
	v_readlane_b32 s1, v254, 3
	s_load_dword s33, s[0:1], 0x0
	s_mov_b32 s61, s96
	s_mov_b32 s0, 24
	s_waitcnt lgkmcnt(0)
	s_ashr_i32 s1, s0, 31
	s_lshl_b64 s[0:1], s[0:1], 3
	s_add_u32 s0, s92, s0
	s_addc_u32 s1, s93, s1
	s_load_dwordx2 s[18:19], s[0:1], 0x0
	s_movk_i32 s0, 0xa0
	v_cmp_gt_i32_e32 vcc, s0, v0
	s_and_saveexec_b64 s[0:1], vcc
	s_cbranch_execz .LBB0_1694
	s_waitcnt lgkmcnt(0)
	global_load_dword v1, v177, s[18:19] offset:384
	v_mov_b32_e32 v2, 0x2100
	global_load_dword v2, v2, s[18:19] offset:384
	v_mov_b32_e32 v3, 0x4200
	global_load_dword v3, v3, s[18:19] offset:384
	v_mov_b32_e32 v4, 0x6300
	global_load_dword v4, v4, s[18:19] offset:384
	v_mov_b32_e32 v5, 0x8400
	global_load_dword v5, v5, s[18:19] offset:384
	v_mov_b32_e32 v6, 0xa500
	global_load_dword v6, v6, s[18:19] offset:384
	v_mov_b32_e32 v7, 0xc600
	global_load_dword v7, v7, s[18:19] offset:384
	v_mov_b32_e32 v8, 0xe700
	global_load_dword v8, v8, s[18:19] offset:384
	v_cmp_eq_u32_e32 vcc, 0, v0
	s_and_saveexec_b64 s[2:3], vcc
	s_cbranch_execz .LBB0_1678
	v_readlane_b32 s4, v254, 57
	s_nop 1
	v_mov_b32_e32 v9, s4
	v_readlane_b32 s4, v254, 58
	s_waitcnt vmcnt(7)
	ds_write_b32 v9, v1
	v_mov_b32_e32 v9, s4
	ds_write_b32 v9, v177
.LBB0_1678:
	s_or_b64 exec, exec, s[2:3]
	s_waitcnt vmcnt(7)
	v_add_u32_e32 v1, 0xff, v1
	v_ashrrev_i32_e32 v1, 8, v1
	v_cmp_eq_u32_e32 vcc, 1, v0
	s_and_saveexec_b64 s[2:3], vcc
	s_cbranch_execz .LBB0_1680
	v_readlane_b32 s4, v254, 59
	s_nop 1
	v_mov_b32_e32 v9, s4
	v_readlane_b32 s4, v254, 60
	s_waitcnt vmcnt(6)
	ds_write_b32 v9, v2
	v_mov_b32_e32 v9, s4
	ds_write_b32 v9, v1
.LBB0_1680:
	s_or_b64 exec, exec, s[2:3]
	s_waitcnt vmcnt(6)
	v_add_u32_e32 v2, 0xff, v2
	v_ashrrev_i32_e32 v2, 8, v2
	v_add_u32_e32 v2, v2, v1
	v_cmp_eq_u32_e32 vcc, 2, v0
	s_and_saveexec_b64 s[2:3], vcc
	s_cbranch_execz .LBB0_1682
	v_readlane_b32 s4, v254, 61
	s_nop 1
	v_mov_b32_e32 v9, s4
	v_readlane_b32 s4, v254, 62
	s_waitcnt vmcnt(5)
	ds_write_b32 v9, v3
	v_mov_b32_e32 v9, s4
	ds_write_b32 v9, v2
.LBB0_1682:
	s_or_b64 exec, exec, s[2:3]
	s_waitcnt vmcnt(5)
	v_add_u32_e32 v3, 0xff, v3
	v_ashrrev_i32_e32 v3, 8, v3
	v_add_u32_e32 v3, v3, v2
	v_cmp_eq_u32_e32 vcc, 3, v0
	s_and_saveexec_b64 s[2:3], vcc
	s_cbranch_execz .LBB0_1684
	v_readlane_b32 s4, v254, 63
	s_nop 1
	v_mov_b32_e32 v9, s4
	v_readlane_b32 s4, v255, 0
	s_waitcnt vmcnt(4)
	ds_write_b32 v9, v4
	v_mov_b32_e32 v9, s4
	ds_write_b32 v9, v3
.LBB0_1684:
	s_or_b64 exec, exec, s[2:3]
	s_waitcnt vmcnt(4)
	v_add_u32_e32 v4, 0xff, v4
	v_ashrrev_i32_e32 v4, 8, v4
	v_add_u32_e32 v4, v4, v3
	v_cmp_eq_u32_e32 vcc, 4, v0
	s_and_saveexec_b64 s[2:3], vcc
	s_cbranch_execz .LBB0_1686
	v_readlane_b32 s4, v255, 1
	s_nop 1
	v_mov_b32_e32 v9, s4
	v_readlane_b32 s4, v255, 2
	s_waitcnt vmcnt(3)
	ds_write_b32 v9, v5
	v_mov_b32_e32 v9, s4
	ds_write_b32 v9, v4
.LBB0_1686:
	s_or_b64 exec, exec, s[2:3]
	s_waitcnt vmcnt(3)
	v_add_u32_e32 v5, 0xff, v5
	v_ashrrev_i32_e32 v5, 8, v5
	v_add_u32_e32 v5, v5, v4
	v_cmp_eq_u32_e32 vcc, 5, v0
	s_and_saveexec_b64 s[2:3], vcc
	s_cbranch_execz .LBB0_1688
	v_readlane_b32 s4, v255, 3
	s_nop 1
	v_mov_b32_e32 v9, s4
	v_readlane_b32 s4, v255, 4
	s_waitcnt vmcnt(2)
	ds_write_b32 v9, v6
	v_mov_b32_e32 v9, s4
	ds_write_b32 v9, v5
.LBB0_1688:
	s_or_b64 exec, exec, s[2:3]
	s_waitcnt vmcnt(2)
	v_add_u32_e32 v6, 0xff, v6
	v_ashrrev_i32_e32 v6, 8, v6
	v_add_u32_e32 v6, v6, v5
	v_cmp_eq_u32_e32 vcc, 6, v0
	s_and_saveexec_b64 s[2:3], vcc
	s_cbranch_execz .LBB0_1690
	v_readlane_b32 s4, v255, 5
	s_nop 1
	v_mov_b32_e32 v9, s4
	v_readlane_b32 s4, v255, 6
	s_waitcnt vmcnt(1)
	ds_write_b32 v9, v7
	v_mov_b32_e32 v9, s4
	ds_write_b32 v9, v6
.LBB0_1690:
	s_or_b64 exec, exec, s[2:3]
	s_waitcnt vmcnt(1)
	v_add_u32_e32 v7, 0xff, v7
	v_ashrrev_i32_e32 v7, 8, v7
	v_add_u32_e32 v7, v7, v6
	v_cmp_eq_u32_e32 vcc, 7, v0
	s_and_saveexec_b64 s[2:3], vcc
	s_cbranch_execz .LBB0_1692
	v_readlane_b32 s4, v255, 7
	s_nop 1
	v_mov_b32_e32 v9, s4
	v_readlane_b32 s4, v255, 8
	s_waitcnt vmcnt(0)
	ds_write_b32 v9, v8
	v_mov_b32_e32 v9, s4
	ds_write_b32 v9, v7

.LBB0_1792:
	s_andn2_b64 vcc, exec, s[0:1]
	s_cbranch_vccnz .LBB0_1880
	v_mbcnt_lo_u32_b32 v0, -1, 0
	v_mbcnt_hi_u32_b32 v0, -1, v0
	v_readlane_b32 s0, v254, 2
	v_add_u32_e32 v0, s79, v0
	v_readlane_b32 s1, v254, 3
	s_load_dword s33, s[0:1], 0x0
	s_mov_b32 s34, s96
	s_mov_b32 s0, 24
	s_waitcnt lgkmcnt(0)
	s_ashr_i32 s1, s0, 31
	s_lshl_b64 s[0:1], s[0:1], 3
	s_add_u32 s0, s92, s0
	s_addc_u32 s1, s93, s1
	s_load_dwordx2 s[2:3], s[0:1], 0x0
	s_movk_i32 s0, 0xa0
	v_cmp_gt_i32_e32 vcc, s0, v0
	s_and_saveexec_b64 s[0:1], vcc
	s_cbranch_execz .LBB0_1812
	s_waitcnt lgkmcnt(0)
	global_load_dword v1, v177, s[2:3] offset:384
	v_mov_b32_e32 v2, 0x2100
	global_load_dword v2, v2, s[2:3] offset:384
	v_mov_b32_e32 v3, 0x4200
	global_load_dword v3, v3, s[2:3] offset:384
	v_mov_b32_e32 v4, 0x6300
	global_load_dword v4, v4, s[2:3] offset:384
	v_mov_b32_e32 v5, 0x8400
	global_load_dword v5, v5, s[2:3] offset:384
	v_mov_b32_e32 v6, 0xa500
	global_load_dword v6, v6, s[2:3] offset:384
	v_mov_b32_e32 v7, 0xc600
	global_load_dword v7, v7, s[2:3] offset:384
	v_mov_b32_e32 v8, 0xe700
	global_load_dword v8, v8, s[2:3] offset:384
	v_cmp_eq_u32_e32 vcc, 0, v0
	s_and_saveexec_b64 s[4:5], vcc
	s_cbranch_execz .LBB0_1796
	v_readlane_b32 s8, v254, 57
	s_nop 1
	v_mov_b32_e32 v9, s8
	v_readlane_b32 s8, v254, 58
	s_waitcnt vmcnt(7)
	ds_write_b32 v9, v1
	v_mov_b32_e32 v9, s8
	ds_write_b32 v9, v177
.LBB0_1796:
	s_or_b64 exec, exec, s[4:5]
	s_waitcnt vmcnt(7)
	v_add_u32_e32 v1, 0xff, v1
	v_ashrrev_i32_e32 v1, 8, v1
	v_cmp_eq_u32_e32 vcc, 1, v0
	s_and_saveexec_b64 s[4:5], vcc
	s_cbranch_execz .LBB0_1798
	v_readlane_b32 s8, v254, 59
	s_nop 1
	v_mov_b32_e32 v9, s8
	v_readlane_b32 s8, v254, 60
	s_waitcnt vmcnt(6)
	ds_write_b32 v9, v2
	v_mov_b32_e32 v9, s8
	ds_write_b32 v9, v1
.LBB0_1798:
	s_or_b64 exec, exec, s[4:5]
	s_waitcnt vmcnt(6)
	v_add_u32_e32 v2, 0xff, v2
	v_ashrrev_i32_e32 v2, 8, v2
	v_add_u32_e32 v2, v2, v1
	v_cmp_eq_u32_e32 vcc, 2, v0
	s_and_saveexec_b64 s[4:5], vcc
	s_cbranch_execz .LBB0_1800
	v_readlane_b32 s8, v254, 61
	s_nop 1
	v_mov_b32_e32 v9, s8
	v_readlane_b32 s8, v254, 62
	s_waitcnt vmcnt(5)
	ds_write_b32 v9, v3
	v_mov_b32_e32 v9, s8
	ds_write_b32 v9, v2
.LBB0_1800:
	s_or_b64 exec, exec, s[4:5]
	s_waitcnt vmcnt(5)
	v_add_u32_e32 v3, 0xff, v3
	v_ashrrev_i32_e32 v3, 8, v3
	v_add_u32_e32 v3, v3, v2
	v_cmp_eq_u32_e32 vcc, 3, v0
	s_and_saveexec_b64 s[4:5], vcc
	s_cbranch_execz .LBB0_1802
	v_readlane_b32 s8, v254, 63
	s_nop 1
	v_mov_b32_e32 v9, s8
	v_readlane_b32 s8, v255, 0
	s_waitcnt vmcnt(4)
	ds_write_b32 v9, v4
	v_mov_b32_e32 v9, s8
	ds_write_b32 v9, v3
.LBB0_1802:
	s_or_b64 exec, exec, s[4:5]
	s_waitcnt vmcnt(4)
	v_add_u32_e32 v4, 0xff, v4
	v_ashrrev_i32_e32 v4, 8, v4
	v_add_u32_e32 v4, v4, v3
	v_cmp_eq_u32_e32 vcc, 4, v0
	s_and_saveexec_b64 s[4:5], vcc
	s_cbranch_execz .LBB0_1804
	v_readlane_b32 s8, v255, 1
	s_nop 1
	v_mov_b32_e32 v9, s8
	v_readlane_b32 s8, v255, 2
	s_waitcnt vmcnt(3)
	ds_write_b32 v9, v5
	v_mov_b32_e32 v9, s8
	ds_write_b32 v9, v4
.LBB0_1804:
	s_or_b64 exec, exec, s[4:5]
	s_waitcnt vmcnt(3)
	v_add_u32_e32 v5, 0xff, v5
	v_ashrrev_i32_e32 v5, 8, v5
	v_add_u32_e32 v5, v5, v4
	v_cmp_eq_u32_e32 vcc, 5, v0
	s_and_saveexec_b64 s[4:5], vcc
	s_cbranch_execz .LBB0_1806
	v_readlane_b32 s8, v255, 3
	s_nop 1
	v_mov_b32_e32 v9, s8
	v_readlane_b32 s8, v255, 4
	s_waitcnt vmcnt(2)
	ds_write_b32 v9, v6
	v_mov_b32_e32 v9, s8
	ds_write_b32 v9, v5
.LBB0_1806:
	s_or_b64 exec, exec, s[4:5]
	s_waitcnt vmcnt(2)
	v_add_u32_e32 v6, 0xff, v6
	v_ashrrev_i32_e32 v6, 8, v6
	v_add_u32_e32 v6, v6, v5
	v_cmp_eq_u32_e32 vcc, 6, v0
	s_and_saveexec_b64 s[4:5], vcc
	s_cbranch_execz .LBB0_1808
	v_readlane_b32 s8, v255, 5
	s_nop 1
	v_mov_b32_e32 v9, s8
	v_readlane_b32 s8, v255, 6
	s_waitcnt vmcnt(1)
	ds_write_b32 v9, v7
	v_mov_b32_e32 v9, s8
	ds_write_b32 v9, v6
.LBB0_1808:
	s_or_b64 exec, exec, s[4:5]
	s_waitcnt vmcnt(1)
	v_add_u32_e32 v7, 0xff, v7
	v_ashrrev_i32_e32 v7, 8, v7
	v_add_u32_e32 v7, v7, v6
	v_cmp_eq_u32_e32 vcc, 7, v0
	s_and_saveexec_b64 s[4:5], vcc
	s_cbranch_execz .LBB0_1810
	v_readlane_b32 s8, v255, 7
	s_nop 1
	v_mov_b32_e32 v9, s8
	v_readlane_b32 s8, v255, 8
	s_waitcnt vmcnt(0)
	ds_write_b32 v9, v8
	v_mov_b32_e32 v9, s8
	ds_write_b32 v9, v7

.LBB0_1883:
	s_lshl_b32 s0, s8, 3
	s_add_i32 s0, s0, s91
	s_mov_b32 s4, 24
	s_mov_b32 s2, 23
	s_cmpk_gt_i32 s0, 0x3fff
	s_cbranch_scc1 .LBB0_1886
	s_ashr_i32 s5, s4, 31
	s_lshl_b64 s[4:5], s[4:5], 3
	s_add_u32 s4, s92, s4
	s_addc_u32 s5, s93, s5
	s_load_dwordx2 s[4:5], s[4:5], 0x0
	v_lshlrev_b32_e32 v0, 3, v2
	v_and_b32_e32 v176, 0x1f8, v0
	s_mov_b64 s[34:35], 0x48600000
	s_waitcnt lgkmcnt(0)
	v_mov_b32_e32 v4, 0x8400
	global_load_dword v4, v4, s[4:5] offset:384
	v_mov_b32_e32 v5, 0xa500
	global_load_dword v5, v5, s[4:5] offset:384
	v_mov_b32_e32 v6, 0xc600
	global_load_dword v6, v6, s[4:5] offset:384
	global_load_dword v8, v177, s[4:5] offset:384
	v_mov_b32_e32 v9, 0x2100
	global_load_dword v9, v9, s[4:5] offset:384
	v_mov_b32_e32 v10, 0x4200
	global_load_dword v10, v10, s[4:5] offset:384
	v_mov_b32_e32 v11, 0x6300
	global_load_dword v11, v11, s[4:5] offset:384
	s_add_u32 s18, s4, 0x440000
	s_addc_u32 s19, s5, 0
	s_ashr_i32 s3, s2, 31
	s_lshl_b64 s[2:3], s[2:3], 3
	s_add_u32 s2, s92, s2
	s_addc_u32 s3, s93, s3
	s_load_dwordx2 s[12:13], s[2:3], 0x0
	v_lshl_add_u64 v[0:1], s[4:5], 0, v[176:177]
	v_lshl_add_u64 v[0:1], v[0:1], 0, s[34:35]
	s_waitcnt vmcnt(4)
	v_readfirstlane_b32 s1, v6
	v_readfirstlane_b32 s2, v5
	v_readfirstlane_b32 s3, v4
	s_addk_i32 s3, 0xff
	s_ashr_i32 s28, s3, 8
	s_addk_i32 s2, 0xff
	s_ashr_i32 s29, s2, 8
	s_addk_i32 s1, 0xff
	s_ashr_i32 s30, s1, 8
	s_lshl_b32 s2, s9, 3
	s_waitcnt vmcnt(0)
	v_readfirstlane_b32 s21, v9
	v_readfirstlane_b32 s20, v8
	v_readfirstlane_b32 s22, v10
	s_addk_i32 s20, 0xff
	s_addk_i32 s21, 0xff
	v_readfirstlane_b32 s23, v11
	s_ashr_i32 s20, s20, 8
	s_ashr_i32 s21, s21, 8
	s_addk_i32 s22, 0xff
	s_add_i32 s21, s21, s20
	s_ashr_i32 s22, s22, 8
	s_addk_i32 s23, 0xff
	s_add_i32 s22, s22, s21
	s_ashr_i32 s23, s23, 8
	s_add_i32 s23, s23, s22
	s_add_i32 s28, s28, s23
	s_add_i32 s29, s29, s28
	s_add_i32 s30, s30, s29
	s_add_u32 s31, s4, 0x420000
	s_addc_u32 s33, s5, 0
	s_ashr_i32 s1, s0, 31
	s_lshl_b64 s[34:35], s[0:1], 12
	v_and_b32_e32 v4, 63, v2
	s_add_u32 s4, s4, s34
	v_lshlrev_b32_e32 v176, 3, v4
	s_addc_u32 s5, s5, s35
	v_lshl_add_u64 v[2:3], s[4:5], 0, v[176:177]
	s_mov_b64 s[4:5], 0x2d000000
	s_ashr_i32 s3, s2, 31
	s_lshl_b32 s8, s8, 4
	v_readlane_b32 s34, v254, 53
	v_lshl_add_u64 v[2:3], v[2:3], 0, s[4:5]
	s_lshl_b64 s[4:5], s[2:3], 12
	s_add_i32 s8, s34, s8
	s_lshl_b32 s34, s9, 4
	s_lshl_b64 s[36:37], s[0:1], 13
	s_waitcnt lgkmcnt(0)
	s_add_u32 s12, s12, s36
	v_lshlrev_b32_e32 v176, 4, v4
	s_addc_u32 s13, s13, s37
	v_lshl_add_u64 v[4:5], s[12:13], 0, v[176:177]
	s_mov_b64 s[12:13], 0x1000
	v_lshl_add_u64 v[4:5], v[4:5], 0, s[12:13]
	s_lshl_b64 s[12:13], s[2:3], 13
	s_ashr_i32 s9, s8, 31
	s_lshl_b64 s[36:37], s[8:9], 2
	s_add_u32 s38, s31, s36
	s_addc_u32 s39, s33, s37
	global_load_dwordx2 v[74:75], v177, s[38:39]
	global_load_dwordx2 v[76:77], v[2:3], off
	global_load_dwordx2 v[78:79], v[2:3], off offset:512
	global_load_dwordx2 v[80:81], v[2:3], off offset:1024
	global_load_dwordx2 v[82:83], v[2:3], off offset:1536
	global_load_dwordx2 v[84:85], v[2:3], off offset:2048
	global_load_dwordx2 v[86:87], v[2:3], off offset:2560
	global_load_dwordx2 v[88:89], v[2:3], off offset:3072
	global_load_dwordx2 v[90:91], v[2:3], off offset:3584
	s_add_i32 s40, s8, 1
	s_ashr_i32 s41, s40, 31
	s_add_u32 s36, s18, s36
	s_addc_u32 s37, s19, s37
	global_load_dword v92, v177, s[36:37]
	s_lshl_b64 s[38:39], s[40:41], 2
	s_add_u32 s36, s18, s38
	s_addc_u32 s37, s19, s39
	global_load_dword v93, v177, s[36:37]
	v_lshl_add_u64 v[2:3], v[2:3], 0, s[4:5]
	s_waitcnt vmcnt(0)
.LBB0_1885:
	s_waitcnt vmcnt(8)
	v_readfirstlane_b32 s1, v74
	v_readfirstlane_b32 s3, v75
	v_mov_b32_e32 v26, v76
	v_mov_b32_e32 v27, v77
	v_mov_b32_e32 v28, v78
	v_mov_b32_e32 v29, v79
	v_mov_b32_e32 v30, v80
	v_mov_b32_e32 v31, v81
	v_mov_b32_e32 v32, v82
	v_mov_b32_e32 v33, v83
	v_mov_b32_e32 v34, v84
	v_mov_b32_e32 v35, v85
	v_mov_b32_e32 v36, v86
	v_mov_b32_e32 v37, v87
	v_mov_b32_e32 v38, v88
	v_mov_b32_e32 v39, v89
	v_mov_b32_e32 v40, v90
	v_mov_b32_e32 v41, v91
	v_mov_b32_e32 v6, v92
	v_mov_b32_e32 v8, v93
	s_ashr_i32 s9, s1, 14
	s_ashr_i32 s35, s3, 14
	s_cmp_eq_u32 s9, 1
	s_cselect_b32 s36, s20, 0
	s_cmp_eq_u32 s35, 1
	s_cselect_b32 s37, s20, 0
	s_cmp_eq_u32 s9, 2
	s_cselect_b32 s36, s21, s36
	s_cmp_eq_u32 s35, 2
	s_cselect_b32 s37, s21, s37
	s_cmp_eq_u32 s9, 3
	s_cselect_b32 s36, s22, s36
	s_cmp_eq_u32 s35, 3
	s_cselect_b32 s37, s22, s37
	s_cmp_eq_u32 s9, 4
	s_cselect_b32 s36, s23, s36
	s_cmp_eq_u32 s35, 4
	s_cselect_b32 s37, s23, s37
	s_cmp_eq_u32 s9, 5
	s_cselect_b32 s36, s28, s36
	s_cmp_eq_u32 s35, 5
	s_cselect_b32 s37, s28, s37
	s_cmp_eq_u32 s9, 6
	s_cselect_b32 s36, s29, s36
	s_cmp_eq_u32 s35, 6
	s_cselect_b32 s37, s29, s37
	s_cmp_eq_u32 s9, 7
	s_cselect_b32 s9, s30, s36
	s_cmp_eq_u32 s35, 7
	s_cselect_b32 s35, s30, s37
	s_lshl_b32 s9, s9, 8
	s_and_b32 s1, s1, 0x3fff
	s_and_b32 s3, s3, 0x3fff
	s_add_i32 s36, s9, s1
	s_lshl_b32 s1, s35, 8
	s_ashr_i32 s37, s36, 31
	s_add_i32 s38, s1, s3
	s_lshl_b64 s[36:37], s[36:37], 12
	s_ashr_i32 s39, s38, 31
	s_lshl_b64 s[38:39], s[38:39], 12
	v_lshl_add_u64 v[10:11], v[0:1], 0, s[36:37]
	v_lshl_add_u64 v[12:13], v[0:1], 0, s[38:39]
	global_load_dwordx2 v[42:43], v[10:11], off
	global_load_dwordx2 v[58:59], v[12:13], off
	global_load_dwordx2 v[44:45], v[10:11], off offset:512
	global_load_dwordx2 v[60:61], v[12:13], off offset:512
	global_load_dwordx2 v[46:47], v[10:11], off offset:1024
	global_load_dwordx2 v[62:63], v[12:13], off offset:1024
	global_load_dwordx2 v[48:49], v[10:11], off offset:1536
	global_load_dwordx2 v[64:65], v[12:13], off offset:1536
	global_load_dwordx2 v[50:51], v[10:11], off offset:2048
	global_load_dwordx2 v[66:67], v[12:13], off offset:2048
	global_load_dwordx2 v[52:53], v[10:11], off offset:2560
	global_load_dwordx2 v[68:69], v[12:13], off offset:2560
	global_load_dwordx2 v[54:55], v[10:11], off offset:3072
	global_load_dwordx2 v[70:71], v[12:13], off offset:3072
	global_load_dwordx2 v[56:57], v[10:11], off offset:3584
	global_load_dwordx2 v[72:73], v[12:13], off offset:3584
	s_add_i32 s0, s0, s2
	s_add_i32 s8, s8, s34
	s_ashr_i32 s9, s8, 31
	s_lshl_b64 s[36:37], s[8:9], 2
	s_add_u32 s38, s31, s36
	s_addc_u32 s39, s33, s37
	global_load_dwordx2 v[74:75], v177, s[38:39]
	global_load_dwordx2 v[76:77], v[2:3], off
	global_load_dwordx2 v[78:79], v[2:3], off offset:512
	global_load_dwordx2 v[80:81], v[2:3], off offset:1024
	global_load_dwordx2 v[82:83], v[2:3], off offset:1536
	global_load_dwordx2 v[84:85], v[2:3], off offset:2048
	global_load_dwordx2 v[86:87], v[2:3], off offset:2560
	global_load_dwordx2 v[88:89], v[2:3], off offset:3072
	global_load_dwordx2 v[90:91], v[2:3], off offset:3584
	s_add_i32 s40, s8, 1
	s_ashr_i32 s41, s40, 31
	s_add_u32 s36, s18, s36
	s_addc_u32 s37, s19, s37
	global_load_dword v92, v177, s[36:37]
	s_lshl_b64 s[38:39], s[40:41], 2
	s_add_u32 s36, s18, s38
	s_addc_u32 s37, s19, s39
	global_load_dword v93, v177, s[36:37]
	v_lshl_add_u64 v[2:3], v[2:3], 0, s[4:5]
	s_cmpk_lt_i32 s0, 0x4000
	s_waitcnt vmcnt(25)
	v_lshlrev_b32_e32 v20, 16, v26
	v_and_b32_e32 v21, 0xffff0000, v26
	v_lshlrev_b32_e32 v22, 16, v42
	v_and_b32_e32 v23, 0xffff0000, v42
	v_lshlrev_b32_e32 v14, 16, v27
	v_and_b32_e32 v15, 0xffff0000, v27
	v_lshlrev_b32_e32 v16, 16, v43
	v_and_b32_e32 v17, 0xffff0000, v43
	v_lshlrev_b32_e32 v24, 16, v58
	v_and_b32_e32 v25, 0xffff0000, v58
	v_lshlrev_b32_e32 v18, 16, v59
	v_and_b32_e32 v19, 0xffff0000, v59
	v_pk_fma_f32 v[20:21], v[6:7], v[22:23], v[20:21] op_sel_hi:[0,1,1]
	v_pk_fma_f32 v[14:15], v[6:7], v[16:17], v[14:15] op_sel_hi:[0,1,1]
	v_pk_fma_f32 v[16:17], v[8:9], v[18:19], v[14:15] op_sel_hi:[0,1,1]
	v_pk_fma_f32 v[14:15], v[8:9], v[24:25], v[20:21] op_sel_hi:[0,1,1]
	global_store_dwordx4 v[4:5], v[14:17], off offset:-4096
	s_waitcnt vmcnt(24)
	v_lshlrev_b32_e32 v20, 16, v28
	v_and_b32_e32 v21, 0xffff0000, v28
	v_lshlrev_b32_e32 v22, 16, v44
	v_and_b32_e32 v23, 0xffff0000, v44
	v_lshlrev_b32_e32 v14, 16, v29
	v_and_b32_e32 v15, 0xffff0000, v29
	v_lshlrev_b32_e32 v16, 16, v45
	v_and_b32_e32 v17, 0xffff0000, v45
	v_lshlrev_b32_e32 v24, 16, v60
	v_and_b32_e32 v25, 0xffff0000, v60
	v_lshlrev_b32_e32 v18, 16, v61
	v_and_b32_e32 v19, 0xffff0000, v61
	v_pk_fma_f32 v[20:21], v[6:7], v[22:23], v[20:21] op_sel_hi:[0,1,1]
	v_pk_fma_f32 v[14:15], v[6:7], v[16:17], v[14:15] op_sel_hi:[0,1,1]
	v_pk_fma_f32 v[16:17], v[8:9], v[18:19], v[14:15] op_sel_hi:[0,1,1]
	v_pk_fma_f32 v[14:15], v[8:9], v[24:25], v[20:21] op_sel_hi:[0,1,1]
	global_store_dwordx4 v[4:5], v[14:17], off offset:-3072
	s_waitcnt vmcnt(23)
	v_lshlrev_b32_e32 v20, 16, v30
	v_and_b32_e32 v21, 0xffff0000, v30
	v_lshlrev_b32_e32 v22, 16, v46
	v_and_b32_e32 v23, 0xffff0000, v46
	v_lshlrev_b32_e32 v14, 16, v31
	v_and_b32_e32 v15, 0xffff0000, v31
	v_lshlrev_b32_e32 v16, 16, v47
	v_and_b32_e32 v17, 0xffff0000, v47
	v_lshlrev_b32_e32 v24, 16, v62
	v_and_b32_e32 v25, 0xffff0000, v62
	v_lshlrev_b32_e32 v18, 16, v63
	v_and_b32_e32 v19, 0xffff0000, v63
	v_pk_fma_f32 v[20:21], v[6:7], v[22:23], v[20:21] op_sel_hi:[0,1,1]
	v_pk_fma_f32 v[14:15], v[6:7], v[16:17], v[14:15] op_sel_hi:[0,1,1]
	v_pk_fma_f32 v[16:17], v[8:9], v[18:19], v[14:15] op_sel_hi:[0,1,1]
	v_pk_fma_f32 v[14:15], v[8:9], v[24:25], v[20:21] op_sel_hi:[0,1,1]
	global_store_dwordx4 v[4:5], v[14:17], off offset:-2048
	s_waitcnt vmcnt(22)
	v_lshlrev_b32_e32 v20, 16, v32
	v_and_b32_e32 v21, 0xffff0000, v32
	v_lshlrev_b32_e32 v22, 16, v48
	v_and_b32_e32 v23, 0xffff0000, v48
	v_lshlrev_b32_e32 v14, 16, v33
	v_and_b32_e32 v15, 0xffff0000, v33
	v_lshlrev_b32_e32 v16, 16, v49
	v_and_b32_e32 v17, 0xffff0000, v49
	v_lshlrev_b32_e32 v24, 16, v64
	v_and_b32_e32 v25, 0xffff0000, v64
	v_lshlrev_b32_e32 v18, 16, v65
	v_and_b32_e32 v19, 0xffff0000, v65
	v_pk_fma_f32 v[20:21], v[6:7], v[22:23], v[20:21] op_sel_hi:[0,1,1]
	v_pk_fma_f32 v[14:15], v[6:7], v[16:17], v[14:15] op_sel_hi:[0,1,1]
	v_pk_fma_f32 v[16:17], v[8:9], v[18:19], v[14:15] op_sel_hi:[0,1,1]
	v_pk_fma_f32 v[14:15], v[8:9], v[24:25], v[20:21] op_sel_hi:[0,1,1]
	global_store_dwordx4 v[4:5], v[14:17], off offset:-1024
	s_waitcnt vmcnt(21)
	v_lshlrev_b32_e32 v20, 16, v34
	v_and_b32_e32 v21, 0xffff0000, v34
	v_lshlrev_b32_e32 v22, 16, v50
	v_and_b32_e32 v23, 0xffff0000, v50
	v_lshlrev_b32_e32 v14, 16, v35
	v_and_b32_e32 v15, 0xffff0000, v35
	v_lshlrev_b32_e32 v16, 16, v51
	v_and_b32_e32 v17, 0xffff0000, v51
	v_lshlrev_b32_e32 v24, 16, v66
	v_and_b32_e32 v25, 0xffff0000, v66
	v_lshlrev_b32_e32 v18, 16, v67
	v_and_b32_e32 v19, 0xffff0000, v67
	v_pk_fma_f32 v[20:21], v[6:7], v[22:23], v[20:21] op_sel_hi:[0,1,1]
	v_pk_fma_f32 v[14:15], v[6:7], v[16:17], v[14:15] op_sel_hi:[0,1,1]
	v_pk_fma_f32 v[16:17], v[8:9], v[18:19], v[14:15] op_sel_hi:[0,1,1]
	v_pk_fma_f32 v[14:15], v[8:9], v[24:25], v[20:21] op_sel_hi:[0,1,1]
	global_store_dwordx4 v[4:5], v[14:17], off
	s_waitcnt vmcnt(20)
	v_lshlrev_b32_e32 v20, 16, v36
	v_and_b32_e32 v21, 0xffff0000, v36
	v_lshlrev_b32_e32 v22, 16, v52
	v_and_b32_e32 v23, 0xffff0000, v52
	v_lshlrev_b32_e32 v14, 16, v37
	v_and_b32_e32 v15, 0xffff0000, v37
	v_lshlrev_b32_e32 v16, 16, v53
	v_and_b32_e32 v17, 0xffff0000, v53
	v_lshlrev_b32_e32 v24, 16, v68
	v_and_b32_e32 v25, 0xffff0000, v68
	v_lshlrev_b32_e32 v18, 16, v69
	v_and_b32_e32 v19, 0xffff0000, v69
	v_pk_fma_f32 v[20:21], v[6:7], v[22:23], v[20:21] op_sel_hi:[0,1,1]
	v_pk_fma_f32 v[14:15], v[6:7], v[16:17], v[14:15] op_sel_hi:[0,1,1]
	v_pk_fma_f32 v[16:17], v[8:9], v[18:19], v[14:15] op_sel_hi:[0,1,1]
	v_pk_fma_f32 v[14:15], v[8:9], v[24:25], v[20:21] op_sel_hi:[0,1,1]
	global_store_dwordx4 v[4:5], v[14:17], off offset:1024
	s_waitcnt vmcnt(19)
	v_lshlrev_b32_e32 v20, 16, v38
	v_and_b32_e32 v21, 0xffff0000, v38
	v_lshlrev_b32_e32 v22, 16, v54
	v_and_b32_e32 v23, 0xffff0000, v54
	v_lshlrev_b32_e32 v14, 16, v39
	v_and_b32_e32 v15, 0xffff0000, v39
	v_lshlrev_b32_e32 v16, 16, v55
	v_and_b32_e32 v17, 0xffff0000, v55
	v_lshlrev_b32_e32 v24, 16, v70
	v_and_b32_e32 v25, 0xffff0000, v70
	v_lshlrev_b32_e32 v18, 16, v71
	v_and_b32_e32 v19, 0xffff0000, v71
	v_pk_fma_f32 v[20:21], v[6:7], v[22:23], v[20:21] op_sel_hi:[0,1,1]
	v_pk_fma_f32 v[14:15], v[6:7], v[16:17], v[14:15] op_sel_hi:[0,1,1]
	v_pk_fma_f32 v[16:17], v[8:9], v[18:19], v[14:15] op_sel_hi:[0,1,1]
	v_pk_fma_f32 v[14:15], v[8:9], v[24:25], v[20:21] op_sel_hi:[0,1,1]
	global_store_dwordx4 v[4:5], v[14:17], off offset:2048
	s_waitcnt vmcnt(18)
	v_lshlrev_b32_e32 v20, 16, v40
	v_and_b32_e32 v21, 0xffff0000, v40
	v_lshlrev_b32_e32 v22, 16, v56
	v_and_b32_e32 v23, 0xffff0000, v56
	v_lshlrev_b32_e32 v14, 16, v41
	v_and_b32_e32 v15, 0xffff0000, v41
	v_lshlrev_b32_e32 v16, 16, v57
	v_and_b32_e32 v17, 0xffff0000, v57
	v_lshlrev_b32_e32 v24, 16, v72
	v_and_b32_e32 v25, 0xffff0000, v72
	v_lshlrev_b32_e32 v18, 16, v73
	v_and_b32_e32 v19, 0xffff0000, v73
	v_pk_fma_f32 v[20:21], v[6:7], v[22:23], v[20:21] op_sel_hi:[0,1,1]
	v_pk_fma_f32 v[14:15], v[6:7], v[16:17], v[14:15] op_sel_hi:[0,1,1]
	v_pk_fma_f32 v[16:17], v[8:9], v[18:19], v[14:15] op_sel_hi:[0,1,1]
	v_pk_fma_f32 v[14:15], v[8:9], v[24:25], v[20:21] op_sel_hi:[0,1,1]
	global_store_dwordx4 v[4:5], v[14:17], off offset:3072
	v_lshl_add_u64 v[4:5], v[4:5], 0, s[12:13]
	s_cbranch_scc1 .LBB0_1885
